# speedup vs baseline: 1.0133x; 1.0133x over previous
.Lk2_noprio:
	s_nop 0
